# SwiGLU epilogues: HID tile stores marked non-temporal (streaming output should not displace the GEMM operand K-slices in L2)
# speedup vs baseline: 1.0044x; 1.0044x over previous
.LBB0_284:
	s_mul_i32 s42, s76, 0x58
	s_lshl_b32 s43, s79, 1
	s_add_i32 s42, s42, s43
	s_or_b32 s42, s42, s71
	s_ashr_i32 s43, s42, 31
	s_lshl_b64 s[42:43], s[42:43], 8
	s_add_u32 s42, s42, s68
	v_mbcnt_lo_u32_b32 v132, -1, 0
	v_mbcnt_hi_u32_b32 v132, -1, v132
	s_addc_u32 s43, s43, s72
	v_and_b32_e32 v133, 15, v132
	v_or_b32_e32 v130, s42, v133
	v_mov_b32_e32 v131, s43
	s_lshl_b32 s42, s74, 10
	v_lshlrev_b64 v[144:145], 7, v[130:131]
	v_ashrrev_i32_e32 v130, 1, v132
	s_add_i32 s42, s73, s42
	v_and_b32_e32 v146, -8, v130
	v_lshl_add_u32 v130, v133, 2, s42
	ds_read2_b32 v[148:149], v130 offset1:16
	ds_read2_b32 v[134:135], v130 offset0:32 offset1:48
	ds_read2_b32 v[132:133], v130 offset0:128 offset1:144
	ds_read2_b32 v[130:131], v130 offset0:160 offset1:176
	v_ashrrev_i32_e32 v147, 31, v146
	v_lshl_add_u64 v[144:145], s[48:49], 0, v[144:145]
	v_lshl_add_u64 v[144:145], v[146:147], 1, v[144:145]
	s_waitcnt lgkmcnt(0)
	v_mul_f32_e32 v146, 0xbfb8aa3b, v148
	v_pk_mul_f32 v[150:151], v[120:121], v[146:147] op_sel_hi:[1,0]
	v_pk_mul_f32 v[152:153], v[118:119], v[146:147] op_sel_hi:[1,0]
	v_pk_mul_f32 v[154:155], v[116:117], v[146:147] op_sel_hi:[1,0]
	v_pk_mul_f32 v[146:147], v[114:115], v[146:147] op_sel_hi:[1,0]
	v_exp_f32_e32 v154, v154
	v_exp_f32_e32 v146, v146
	v_exp_f32_e32 v155, v155
	v_exp_f32_e32 v147, v147
	v_exp_f32_e32 v152, v152
	v_exp_f32_e32 v153, v153
	v_exp_f32_e32 v150, v150
	v_exp_f32_e32 v151, v151
	v_pk_add_f32 v[154:155], v[154:155], 1.0 op_sel_hi:[1,0]
	v_pk_add_f32 v[146:147], v[146:147], 1.0 op_sel_hi:[1,0]
	v_pk_add_f32 v[152:153], v[152:153], 1.0 op_sel_hi:[1,0]
	v_pk_add_f32 v[150:151], v[150:151], 1.0 op_sel_hi:[1,0]
	v_rcp_f32_e32 v146, v146
	v_rcp_f32_e32 v147, v147
	v_rcp_f32_e32 v154, v154
	v_rcp_f32_e32 v155, v155
	v_rcp_f32_e32 v152, v152
	v_rcp_f32_e32 v153, v153
	v_rcp_f32_e32 v150, v150
	v_rcp_f32_e32 v151, v151
	v_mul_f32_e32 v148, v148, v148
	v_pk_mul_f32 v[116:117], v[124:125], v[116:117]
	v_pk_mul_f32 v[114:115], v[122:123], v[114:115]
	v_pk_mul_f32 v[120:121], v[128:129], v[120:121]
	v_pk_mul_f32 v[118:119], v[126:127], v[118:119]
	v_pk_mul_f32 v[116:117], v[116:117], v[148:149] op_sel_hi:[1,0]
	v_pk_mul_f32 v[114:115], v[114:115], v[148:149] op_sel_hi:[1,0]
	v_pk_mul_f32 v[120:121], v[120:121], v[148:149] op_sel_hi:[1,0]
	v_pk_mul_f32 v[118:119], v[118:119], v[148:149] op_sel_hi:[1,0]
	v_pk_mul_f32 v[122:123], v[116:117], v[154:155]
	v_pk_mul_f32 v[116:117], v[114:115], v[146:147]
	v_pk_mul_f32 v[120:121], v[120:121], v[150:151]
	v_pk_mul_f32 v[118:119], v[118:119], v[152:153]
	v_mul_f32_e32 v124, v149, v149
	v_cvt_pk_bf16_f32 v114, v118, v119
	v_cvt_pk_bf16_f32 v115, v120, v121
	v_cvt_pk_bf16_f32 v116, v116, v117
	v_cvt_pk_bf16_f32 v117, v122, v123
	global_store_dwordx4 v[144:145], v[114:117], off nt
	s_mov_b64 s[42:43], 0x2000
	s_and_b64 vcc, exec, s[40:41]
	v_mul_f32_e32 v116, 0xbfb8aa3b, v149
	v_pk_mul_f32 v[118:119], v[104:105], v[116:117] op_sel_hi:[1,0]
	v_pk_mul_f32 v[120:121], v[102:103], v[116:117] op_sel_hi:[1,0]
	v_pk_mul_f32 v[122:123], v[100:101], v[116:117] op_sel_hi:[1,0]
	v_pk_mul_f32 v[116:117], v[98:99], v[116:117] op_sel_hi:[1,0]
	v_exp_f32_e32 v122, v122
	v_exp_f32_e32 v116, v116
	v_exp_f32_e32 v123, v123
	v_exp_f32_e32 v117, v117
	v_exp_f32_e32 v120, v120
	v_exp_f32_e32 v121, v121
	v_exp_f32_e32 v118, v118
	v_exp_f32_e32 v119, v119
	v_pk_add_f32 v[122:123], v[122:123], 1.0 op_sel_hi:[1,0]
	v_pk_add_f32 v[116:117], v[116:117], 1.0 op_sel_hi:[1,0]
	v_pk_add_f32 v[120:121], v[120:121], 1.0 op_sel_hi:[1,0]
	v_pk_add_f32 v[118:119], v[118:119], 1.0 op_sel_hi:[1,0]
	v_rcp_f32_e32 v116, v116
	v_rcp_f32_e32 v117, v117
	v_rcp_f32_e32 v122, v122
	v_rcp_f32_e32 v123, v123
	v_rcp_f32_e32 v120, v120
	v_rcp_f32_e32 v121, v121
	v_rcp_f32_e32 v118, v118
	v_rcp_f32_e32 v119, v119
	v_pk_mul_f32 v[100:101], v[108:109], v[100:101]
	v_pk_mul_f32 v[98:99], v[106:107], v[98:99]
	v_pk_mul_f32 v[104:105], v[112:113], v[104:105]
	v_pk_mul_f32 v[102:103], v[110:111], v[102:103]
	v_pk_mul_f32 v[100:101], v[100:101], v[124:125] op_sel_hi:[1,0]
	v_pk_mul_f32 v[98:99], v[98:99], v[124:125] op_sel_hi:[1,0]
	v_lshl_add_u64 v[114:115], v[144:145], 0, s[12:13]
	v_pk_mul_f32 v[104:105], v[104:105], v[124:125] op_sel_hi:[1,0]
	v_pk_mul_f32 v[102:103], v[102:103], v[124:125] op_sel_hi:[1,0]
	v_pk_mul_f32 v[106:107], v[100:101], v[122:123]
	v_pk_mul_f32 v[100:101], v[98:99], v[116:117]
	v_pk_mul_f32 v[104:105], v[104:105], v[118:119]
	v_pk_mul_f32 v[102:103], v[102:103], v[120:121]
	v_mul_f32_e32 v108, v134, v134
	v_cvt_pk_bf16_f32 v98, v102, v103
	v_cvt_pk_bf16_f32 v99, v104, v105
	v_cvt_pk_bf16_f32 v100, v100, v101
	v_cvt_pk_bf16_f32 v101, v106, v107
	global_store_dwordx4 v[114:115], v[98:101], off nt
	s_mov_b64 s[40:41], -1
	s_nop 0
	v_mul_f32_e32 v100, 0xbfb8aa3b, v134
	v_pk_mul_f32 v[102:103], v[88:89], v[100:101] op_sel_hi:[1,0]
	v_pk_mul_f32 v[104:105], v[86:87], v[100:101] op_sel_hi:[1,0]
	v_pk_mul_f32 v[106:107], v[84:85], v[100:101] op_sel_hi:[1,0]
	v_pk_mul_f32 v[100:101], v[82:83], v[100:101] op_sel_hi:[1,0]
	v_exp_f32_e32 v106, v106
	v_exp_f32_e32 v100, v100
	v_exp_f32_e32 v107, v107
	v_exp_f32_e32 v101, v101
	v_exp_f32_e32 v104, v104
	v_exp_f32_e32 v105, v105
	v_exp_f32_e32 v102, v102
	v_exp_f32_e32 v103, v103
	v_pk_add_f32 v[106:107], v[106:107], 1.0 op_sel_hi:[1,0]
	v_pk_add_f32 v[100:101], v[100:101], 1.0 op_sel_hi:[1,0]
	v_pk_add_f32 v[104:105], v[104:105], 1.0 op_sel_hi:[1,0]
	v_pk_add_f32 v[102:103], v[102:103], 1.0 op_sel_hi:[1,0]
	v_rcp_f32_e32 v100, v100
	v_rcp_f32_e32 v101, v101
	v_rcp_f32_e32 v106, v106
	v_rcp_f32_e32 v107, v107
	v_rcp_f32_e32 v104, v104
	v_rcp_f32_e32 v105, v105
	v_rcp_f32_e32 v102, v102
	v_rcp_f32_e32 v103, v103
	v_pk_mul_f32 v[84:85], v[92:93], v[84:85]
	v_pk_mul_f32 v[82:83], v[90:91], v[82:83]
	v_pk_mul_f32 v[88:89], v[96:97], v[88:89]
	v_pk_mul_f32 v[86:87], v[94:95], v[86:87]
	v_pk_mul_f32 v[84:85], v[84:85], v[108:109] op_sel_hi:[1,0]
	v_pk_mul_f32 v[82:83], v[82:83], v[108:109] op_sel_hi:[1,0]
	v_lshl_add_u64 v[98:99], v[114:115], 0, s[12:13]
	v_pk_mul_f32 v[88:89], v[88:89], v[108:109] op_sel_hi:[1,0]
	v_pk_mul_f32 v[86:87], v[86:87], v[108:109] op_sel_hi:[1,0]
	v_pk_mul_f32 v[90:91], v[84:85], v[106:107]
	v_pk_mul_f32 v[84:85], v[82:83], v[100:101]
	v_pk_mul_f32 v[88:89], v[88:89], v[102:103]
	v_pk_mul_f32 v[86:87], v[86:87], v[104:105]
	v_mul_f32_e32 v92, v135, v135
	v_cvt_pk_bf16_f32 v82, v86, v87
	v_cvt_pk_bf16_f32 v83, v88, v89
	v_cvt_pk_bf16_f32 v84, v84, v85
	v_cvt_pk_bf16_f32 v85, v90, v91
	global_store_dwordx4 v[98:99], v[82:85], off nt
	s_nop 1
	v_mul_f32_e32 v84, 0xbfb8aa3b, v135
	v_pk_mul_f32 v[86:87], v[64:65], v[84:85] op_sel_hi:[1,0]
	v_pk_mul_f32 v[88:89], v[62:63], v[84:85] op_sel_hi:[1,0]
	v_pk_mul_f32 v[90:91], v[56:57], v[84:85] op_sel_hi:[1,0]
	v_pk_mul_f32 v[84:85], v[54:55], v[84:85] op_sel_hi:[1,0]
	v_exp_f32_e32 v90, v90
	v_exp_f32_e32 v84, v84
	v_exp_f32_e32 v91, v91
	v_exp_f32_e32 v85, v85
	v_exp_f32_e32 v88, v88
	v_exp_f32_e32 v89, v89
	v_exp_f32_e32 v86, v86
	v_exp_f32_e32 v87, v87
	v_pk_add_f32 v[90:91], v[90:91], 1.0 op_sel_hi:[1,0]
	v_pk_add_f32 v[84:85], v[84:85], 1.0 op_sel_hi:[1,0]
	v_pk_add_f32 v[88:89], v[88:89], 1.0 op_sel_hi:[1,0]
	v_pk_add_f32 v[86:87], v[86:87], 1.0 op_sel_hi:[1,0]
	v_rcp_f32_e32 v84, v84
	v_rcp_f32_e32 v85, v85
	v_rcp_f32_e32 v90, v90
	v_rcp_f32_e32 v91, v91
	v_rcp_f32_e32 v88, v88
	v_rcp_f32_e32 v89, v89
	v_rcp_f32_e32 v86, v86
	v_rcp_f32_e32 v87, v87
	v_pk_mul_f32 v[56:57], v[72:73], v[56:57]
	v_pk_mul_f32 v[54:55], v[70:71], v[54:55]
	v_pk_mul_f32 v[64:65], v[80:81], v[64:65]
	v_pk_mul_f32 v[62:63], v[78:79], v[62:63]
	v_pk_mul_f32 v[56:57], v[56:57], v[92:93] op_sel_hi:[1,0]
	v_pk_mul_f32 v[54:55], v[54:55], v[92:93] op_sel_hi:[1,0]
	v_lshl_add_u64 v[82:83], v[98:99], 0, s[12:13]
	v_pk_mul_f32 v[64:65], v[64:65], v[92:93] op_sel_hi:[1,0]
	v_pk_mul_f32 v[62:63], v[62:63], v[92:93] op_sel_hi:[1,0]
	v_pk_mul_f32 v[70:71], v[56:57], v[90:91]
	v_pk_mul_f32 v[56:57], v[54:55], v[84:85]
	v_pk_mul_f32 v[64:65], v[64:65], v[86:87]
	v_pk_mul_f32 v[62:63], v[62:63], v[88:89]
	v_mul_f32_e32 v72, v132, v132
	v_cvt_pk_bf16_f32 v54, v62, v63
	v_cvt_pk_bf16_f32 v55, v64, v65
	v_cvt_pk_bf16_f32 v56, v56, v57
	v_cvt_pk_bf16_f32 v57, v70, v71
	global_store_dwordx4 v[82:83], v[54:57], off nt
	s_nop 1
	v_mul_f32_e32 v56, 0xbfb8aa3b, v132
	v_pk_mul_f32 v[62:63], v[60:61], v[56:57] op_sel_hi:[1,0]
	v_pk_mul_f32 v[64:65], v[58:59], v[56:57] op_sel_hi:[1,0]
	v_pk_mul_f32 v[70:71], v[52:53], v[56:57] op_sel_hi:[1,0]
	v_pk_mul_f32 v[56:57], v[50:51], v[56:57] op_sel_hi:[1,0]
	v_exp_f32_e32 v62, v62
	v_exp_f32_e32 v56, v56
	v_exp_f32_e32 v63, v63
	v_exp_f32_e32 v70, v70
	v_exp_f32_e32 v71, v71
	v_exp_f32_e32 v57, v57
	v_exp_f32_e32 v64, v64
	v_exp_f32_e32 v65, v65
	v_pk_add_f32 v[62:63], v[62:63], 1.0 op_sel_hi:[1,0]
	v_pk_add_f32 v[70:71], v[70:71], 1.0 op_sel_hi:[1,0]
	v_pk_add_f32 v[56:57], v[56:57], 1.0 op_sel_hi:[1,0]
	v_pk_add_f32 v[64:65], v[64:65], 1.0 op_sel_hi:[1,0]
	v_rcp_f32_e32 v56, v56
	v_rcp_f32_e32 v57, v57
	v_rcp_f32_e32 v62, v62
	v_rcp_f32_e32 v70, v70
	v_rcp_f32_e32 v63, v63
	v_rcp_f32_e32 v71, v71
	v_rcp_f32_e32 v64, v64
	v_rcp_f32_e32 v65, v65
	v_lshl_add_u64 v[54:55], v[82:83], 0, s[12:13]
	v_pk_mul_f32 v[60:61], v[76:77], v[60:61]
	v_pk_mul_f32 v[52:53], v[68:69], v[52:53]
	v_pk_mul_f32 v[50:51], v[66:67], v[50:51]
	v_pk_mul_f32 v[58:59], v[74:75], v[58:59]
	v_pk_mul_f32 v[60:61], v[60:61], v[72:73] op_sel_hi:[1,0]
	v_pk_mul_f32 v[52:53], v[52:53], v[72:73] op_sel_hi:[1,0]
	v_pk_mul_f32 v[50:51], v[50:51], v[72:73] op_sel_hi:[1,0]
	v_lshl_add_u64 v[54:55], v[54:55], 0, s[42:43]
	v_pk_mul_f32 v[58:59], v[58:59], v[72:73] op_sel_hi:[1,0]
	v_pk_mul_f32 v[60:61], v[60:61], v[62:63]
	v_pk_mul_f32 v[62:63], v[52:53], v[70:71]
	v_pk_mul_f32 v[52:53], v[50:51], v[56:57]
	v_pk_mul_f32 v[58:59], v[58:59], v[64:65]
	s_nop 0
	v_cvt_pk_bf16_f32 v50, v58, v59
	v_cvt_pk_bf16_f32 v51, v60, v61
	v_cvt_pk_bf16_f32 v52, v52, v53
	v_cvt_pk_bf16_f32 v53, v62, v63
	global_store_dwordx4 v[54:55], v[50:53], off nt
	v_mul_f32_e32 v60, v133, v133
	s_nop 0
	v_mul_f32_e32 v52, 0xbfb8aa3b, v133
	v_lshl_add_u64 v[50:51], v[54:55], 0, s[12:13]
	v_pk_mul_f32 v[54:55], v[40:41], v[52:53] op_sel_hi:[1,0]
	v_pk_mul_f32 v[56:57], v[38:39], v[52:53] op_sel_hi:[1,0]
	v_pk_mul_f32 v[58:59], v[36:37], v[52:53] op_sel_hi:[1,0]
	v_pk_mul_f32 v[52:53], v[34:35], v[52:53] op_sel_hi:[1,0]
	v_exp_f32_e32 v58, v58
	v_exp_f32_e32 v52, v52
	v_exp_f32_e32 v59, v59
	v_exp_f32_e32 v53, v53
	v_exp_f32_e32 v56, v56
	v_exp_f32_e32 v57, v57
	v_exp_f32_e32 v54, v54
	v_exp_f32_e32 v55, v55
	v_pk_add_f32 v[58:59], v[58:59], 1.0 op_sel_hi:[1,0]
	v_pk_add_f32 v[52:53], v[52:53], 1.0 op_sel_hi:[1,0]
	v_pk_add_f32 v[56:57], v[56:57], 1.0 op_sel_hi:[1,0]
	v_pk_add_f32 v[54:55], v[54:55], 1.0 op_sel_hi:[1,0]
	v_rcp_f32_e32 v52, v52
	v_rcp_f32_e32 v53, v53
	v_rcp_f32_e32 v58, v58
	v_rcp_f32_e32 v59, v59
	v_rcp_f32_e32 v56, v56
	v_rcp_f32_e32 v57, v57
	v_rcp_f32_e32 v54, v54
	v_rcp_f32_e32 v55, v55
	v_pk_mul_f32 v[36:37], v[44:45], v[36:37]
	v_pk_mul_f32 v[34:35], v[42:43], v[34:35]
	v_pk_mul_f32 v[40:41], v[48:49], v[40:41]
	v_pk_mul_f32 v[38:39], v[46:47], v[38:39]
	v_pk_mul_f32 v[36:37], v[36:37], v[60:61] op_sel_hi:[1,0]
	v_pk_mul_f32 v[34:35], v[34:35], v[60:61] op_sel_hi:[1,0]
	v_pk_mul_f32 v[40:41], v[40:41], v[60:61] op_sel_hi:[1,0]
	v_pk_mul_f32 v[38:39], v[38:39], v[60:61] op_sel_hi:[1,0]
	v_pk_mul_f32 v[42:43], v[36:37], v[58:59]
	v_pk_mul_f32 v[36:37], v[34:35], v[52:53]
	v_pk_mul_f32 v[40:41], v[40:41], v[54:55]
	v_pk_mul_f32 v[38:39], v[38:39], v[56:57]
	v_mul_f32_e32 v44, v130, v130
	v_cvt_pk_bf16_f32 v34, v38, v39
	v_cvt_pk_bf16_f32 v35, v40, v41
	v_cvt_pk_bf16_f32 v36, v36, v37
	v_cvt_pk_bf16_f32 v37, v42, v43
	global_store_dwordx4 v[50:51], v[34:37], off nt
	s_nop 1
	v_mul_f32_e32 v36, 0xbfb8aa3b, v130
	v_pk_mul_f32 v[38:39], v[24:25], v[36:37] op_sel_hi:[1,0]
	v_pk_mul_f32 v[40:41], v[22:23], v[36:37] op_sel_hi:[1,0]
	v_pk_mul_f32 v[42:43], v[20:21], v[36:37] op_sel_hi:[1,0]
	v_pk_mul_f32 v[36:37], v[18:19], v[36:37] op_sel_hi:[1,0]
	v_exp_f32_e32 v42, v42
	v_exp_f32_e32 v36, v36
	v_exp_f32_e32 v43, v43
	v_exp_f32_e32 v37, v37
	v_exp_f32_e32 v40, v40
	v_exp_f32_e32 v41, v41
	v_exp_f32_e32 v38, v38
	v_exp_f32_e32 v39, v39
	v_pk_add_f32 v[42:43], v[42:43], 1.0 op_sel_hi:[1,0]
	v_pk_add_f32 v[36:37], v[36:37], 1.0 op_sel_hi:[1,0]
	v_pk_add_f32 v[40:41], v[40:41], 1.0 op_sel_hi:[1,0]
	v_pk_add_f32 v[38:39], v[38:39], 1.0 op_sel_hi:[1,0]
	v_rcp_f32_e32 v36, v36
	v_rcp_f32_e32 v37, v37
	v_rcp_f32_e32 v42, v42
	v_rcp_f32_e32 v43, v43
	v_rcp_f32_e32 v40, v40
	v_rcp_f32_e32 v41, v41
	v_rcp_f32_e32 v38, v38
	v_rcp_f32_e32 v39, v39
	v_pk_mul_f32 v[20:21], v[28:29], v[20:21]
	v_pk_mul_f32 v[18:19], v[26:27], v[18:19]
	v_pk_mul_f32 v[24:25], v[32:33], v[24:25]
	v_pk_mul_f32 v[22:23], v[30:31], v[22:23]
	v_pk_mul_f32 v[20:21], v[20:21], v[44:45] op_sel_hi:[1,0]
	v_pk_mul_f32 v[18:19], v[18:19], v[44:45] op_sel_hi:[1,0]
	v_lshl_add_u64 v[34:35], v[50:51], 0, s[12:13]
	v_pk_mul_f32 v[24:25], v[24:25], v[44:45] op_sel_hi:[1,0]
	v_pk_mul_f32 v[22:23], v[22:23], v[44:45] op_sel_hi:[1,0]
	v_pk_mul_f32 v[26:27], v[20:21], v[42:43]
	v_pk_mul_f32 v[20:21], v[18:19], v[36:37]
	v_pk_mul_f32 v[24:25], v[24:25], v[38:39]
	v_pk_mul_f32 v[22:23], v[22:23], v[40:41]
	v_mul_f32_e32 v28, v131, v131
	v_cvt_pk_bf16_f32 v18, v22, v23
	v_cvt_pk_bf16_f32 v19, v24, v25
	v_cvt_pk_bf16_f32 v20, v20, v21
	v_cvt_pk_bf16_f32 v21, v26, v27
	global_store_dwordx4 v[34:35], v[18:21], off nt
	s_nop 1
	v_mul_f32_e32 v20, 0xbfb8aa3b, v131
	v_pk_mul_f32 v[22:23], v[8:9], v[20:21] op_sel_hi:[1,0]
	v_pk_mul_f32 v[24:25], v[6:7], v[20:21] op_sel_hi:[1,0]
	v_pk_mul_f32 v[26:27], v[4:5], v[20:21] op_sel_hi:[1,0]
	v_pk_mul_f32 v[20:21], v[2:3], v[20:21] op_sel_hi:[1,0]
	v_exp_f32_e32 v24, v24
	v_exp_f32_e32 v20, v20
	v_exp_f32_e32 v25, v25
	v_exp_f32_e32 v22, v22
	v_exp_f32_e32 v23, v23
	v_exp_f32_e32 v26, v26
	v_exp_f32_e32 v27, v27
	v_exp_f32_e32 v21, v21
	v_pk_add_f32 v[22:23], v[22:23], 1.0 op_sel_hi:[1,0]
	v_pk_add_f32 v[24:25], v[24:25], 1.0 op_sel_hi:[1,0]
	v_pk_add_f32 v[26:27], v[26:27], 1.0 op_sel_hi:[1,0]
	v_pk_add_f32 v[20:21], v[20:21], 1.0 op_sel_hi:[1,0]
	v_rcp_f32_e32 v24, v24
	v_rcp_f32_e32 v20, v20
	v_rcp_f32_e32 v25, v25
	v_rcp_f32_e32 v21, v21
	v_rcp_f32_e32 v22, v22
	v_rcp_f32_e32 v26, v26
	v_rcp_f32_e32 v23, v23
	v_rcp_f32_e32 v27, v27
	v_pk_mul_f32 v[8:9], v[16:17], v[8:9]
	v_pk_mul_f32 v[6:7], v[14:15], v[6:7]
	v_pk_mul_f32 v[4:5], v[12:13], v[4:5]
	v_pk_mul_f32 v[2:3], v[10:11], v[2:3]
	v_lshl_add_u64 v[18:19], v[34:35], 0, s[12:13]
	v_pk_mul_f32 v[8:9], v[8:9], v[28:29] op_sel_hi:[1,0]
	v_pk_mul_f32 v[6:7], v[6:7], v[28:29] op_sel_hi:[1,0]
	v_pk_mul_f32 v[4:5], v[4:5], v[28:29] op_sel_hi:[1,0]
	v_pk_mul_f32 v[2:3], v[2:3], v[28:29] op_sel_hi:[1,0]
	v_pk_mul_f32 v[8:9], v[8:9], v[22:23]
	v_pk_mul_f32 v[6:7], v[6:7], v[24:25]
	v_pk_mul_f32 v[10:11], v[4:5], v[26:27]
	v_pk_mul_f32 v[4:5], v[2:3], v[20:21]
	v_cvt_pk_bf16_f32 v2, v6, v7
	v_cvt_pk_bf16_f32 v3, v8, v9
	s_nop 0
	v_cvt_pk_bf16_f32 v4, v4, v5
	v_cvt_pk_bf16_f32 v5, v10, v11
	global_store_dwordx4 v[18:19], v[2:5], off nt
	s_nop 1
	v_lshl_add_u64 v[2:3], v[18:19], 0, s[12:13]
	s_nop 0
	v_lshl_add_u64 v[2:3], v[2:3], 0, s[42:43]
	s_cbranch_vccnz .LBB0_267
	s_cmp_lg_u32 s78, s76
	s_cselect_b64 s[40:41], -1, 0
	v_cndmask_b32_e64 v2, 0, 1, s[40:41]
	s_andn2_b64 vcc, exec, s[30:31]
	v_readfirstlane_b32 s40, v2
	s_cbranch_vccnz .LBB0_266
	s_barrier
	s_branch .LBB0_266

.LBB0_1155:
	s_mul_i32 s42, s74, 0x58
	s_lshl_b32 s43, s77, 1
	s_add_i32 s42, s42, s43
	s_or_b32 s42, s42, s69
	s_ashr_i32 s43, s42, 31
	s_lshl_b64 s[42:43], s[42:43], 8
	s_add_u32 s42, s42, s66
	v_mbcnt_lo_u32_b32 v132, -1, 0
	v_mbcnt_hi_u32_b32 v132, -1, v132
	s_addc_u32 s43, s43, s70
	v_and_b32_e32 v133, 15, v132
	v_or_b32_e32 v130, s42, v133
	v_mov_b32_e32 v131, s43
	s_lshl_b32 s42, s72, 10
	v_lshlrev_b64 v[144:145], 7, v[130:131]
	v_ashrrev_i32_e32 v130, 1, v132
	s_add_i32 s42, s71, s42
	v_and_b32_e32 v146, -8, v130
	v_lshl_add_u32 v130, v133, 2, s42
	ds_read2_b32 v[148:149], v130 offset1:16
	ds_read2_b32 v[134:135], v130 offset0:32 offset1:48
	ds_read2_b32 v[132:133], v130 offset0:128 offset1:144
	ds_read2_b32 v[130:131], v130 offset0:160 offset1:176
	v_ashrrev_i32_e32 v147, 31, v146
	v_lshl_add_u64 v[144:145], s[46:47], 0, v[144:145]
	v_lshl_add_u64 v[144:145], v[146:147], 1, v[144:145]
	s_waitcnt lgkmcnt(0)
	v_mul_f32_e32 v146, 0xbfb8aa3b, v148
	v_pk_mul_f32 v[150:151], v[120:121], v[146:147] op_sel_hi:[1,0]
	v_pk_mul_f32 v[152:153], v[118:119], v[146:147] op_sel_hi:[1,0]
	v_pk_mul_f32 v[154:155], v[116:117], v[146:147] op_sel_hi:[1,0]
	v_pk_mul_f32 v[146:147], v[114:115], v[146:147] op_sel_hi:[1,0]
	v_exp_f32_e32 v154, v154
	v_exp_f32_e32 v146, v146
	v_exp_f32_e32 v155, v155
	v_exp_f32_e32 v147, v147
	v_exp_f32_e32 v152, v152
	v_exp_f32_e32 v153, v153
	v_exp_f32_e32 v150, v150
	v_exp_f32_e32 v151, v151
	v_pk_add_f32 v[154:155], v[154:155], 1.0 op_sel_hi:[1,0]
	v_pk_add_f32 v[146:147], v[146:147], 1.0 op_sel_hi:[1,0]
	v_pk_add_f32 v[152:153], v[152:153], 1.0 op_sel_hi:[1,0]
	v_pk_add_f32 v[150:151], v[150:151], 1.0 op_sel_hi:[1,0]
	v_rcp_f32_e32 v146, v146
	v_rcp_f32_e32 v147, v147
	v_rcp_f32_e32 v154, v154
	v_rcp_f32_e32 v155, v155
	v_rcp_f32_e32 v152, v152
	v_rcp_f32_e32 v153, v153
	v_rcp_f32_e32 v150, v150
	v_rcp_f32_e32 v151, v151
	v_mul_f32_e32 v148, v148, v148
	v_pk_mul_f32 v[116:117], v[124:125], v[116:117]
	v_pk_mul_f32 v[114:115], v[122:123], v[114:115]
	v_pk_mul_f32 v[120:121], v[128:129], v[120:121]
	v_pk_mul_f32 v[118:119], v[126:127], v[118:119]
	v_pk_mul_f32 v[116:117], v[116:117], v[148:149] op_sel_hi:[1,0]
	v_pk_mul_f32 v[114:115], v[114:115], v[148:149] op_sel_hi:[1,0]
	v_pk_mul_f32 v[120:121], v[120:121], v[148:149] op_sel_hi:[1,0]
	v_pk_mul_f32 v[118:119], v[118:119], v[148:149] op_sel_hi:[1,0]
	v_pk_mul_f32 v[122:123], v[116:117], v[154:155]
	v_pk_mul_f32 v[116:117], v[114:115], v[146:147]
	v_pk_mul_f32 v[120:121], v[120:121], v[150:151]
	v_pk_mul_f32 v[118:119], v[118:119], v[152:153]
	v_mul_f32_e32 v124, v149, v149
	v_cvt_pk_bf16_f32 v114, v118, v119
	v_cvt_pk_bf16_f32 v115, v120, v121
	v_cvt_pk_bf16_f32 v116, v116, v117
	v_cvt_pk_bf16_f32 v117, v122, v123
	global_store_dwordx4 v[144:145], v[114:117], off nt
	s_mov_b64 s[42:43], 0x2000
	s_and_b64 vcc, exec, s[40:41]
	v_mul_f32_e32 v116, 0xbfb8aa3b, v149
	v_pk_mul_f32 v[118:119], v[104:105], v[116:117] op_sel_hi:[1,0]
	v_pk_mul_f32 v[120:121], v[102:103], v[116:117] op_sel_hi:[1,0]
	v_pk_mul_f32 v[122:123], v[100:101], v[116:117] op_sel_hi:[1,0]
	v_pk_mul_f32 v[116:117], v[98:99], v[116:117] op_sel_hi:[1,0]
	v_exp_f32_e32 v122, v122
	v_exp_f32_e32 v116, v116
	v_exp_f32_e32 v123, v123
	v_exp_f32_e32 v117, v117
	v_exp_f32_e32 v120, v120
	v_exp_f32_e32 v121, v121
	v_exp_f32_e32 v118, v118
	v_exp_f32_e32 v119, v119
	v_pk_add_f32 v[122:123], v[122:123], 1.0 op_sel_hi:[1,0]
	v_pk_add_f32 v[116:117], v[116:117], 1.0 op_sel_hi:[1,0]
	v_pk_add_f32 v[120:121], v[120:121], 1.0 op_sel_hi:[1,0]
	v_pk_add_f32 v[118:119], v[118:119], 1.0 op_sel_hi:[1,0]
	v_rcp_f32_e32 v116, v116
	v_rcp_f32_e32 v117, v117
	v_rcp_f32_e32 v122, v122
	v_rcp_f32_e32 v123, v123
	v_rcp_f32_e32 v120, v120
	v_rcp_f32_e32 v121, v121
	v_rcp_f32_e32 v118, v118
	v_rcp_f32_e32 v119, v119
	v_pk_mul_f32 v[100:101], v[108:109], v[100:101]
	v_pk_mul_f32 v[98:99], v[106:107], v[98:99]
	v_pk_mul_f32 v[104:105], v[112:113], v[104:105]
	v_pk_mul_f32 v[102:103], v[110:111], v[102:103]
	v_pk_mul_f32 v[100:101], v[100:101], v[124:125] op_sel_hi:[1,0]
	v_pk_mul_f32 v[98:99], v[98:99], v[124:125] op_sel_hi:[1,0]
	v_lshl_add_u64 v[114:115], v[144:145], 0, s[12:13]
	v_pk_mul_f32 v[104:105], v[104:105], v[124:125] op_sel_hi:[1,0]
	v_pk_mul_f32 v[102:103], v[102:103], v[124:125] op_sel_hi:[1,0]
	v_pk_mul_f32 v[106:107], v[100:101], v[122:123]
	v_pk_mul_f32 v[100:101], v[98:99], v[116:117]
	v_pk_mul_f32 v[104:105], v[104:105], v[118:119]
	v_pk_mul_f32 v[102:103], v[102:103], v[120:121]
	v_mul_f32_e32 v108, v134, v134
	v_cvt_pk_bf16_f32 v98, v102, v103
	v_cvt_pk_bf16_f32 v99, v104, v105
	v_cvt_pk_bf16_f32 v100, v100, v101
	v_cvt_pk_bf16_f32 v101, v106, v107
	global_store_dwordx4 v[114:115], v[98:101], off nt
	s_mov_b64 s[40:41], -1
	s_nop 0
	v_mul_f32_e32 v100, 0xbfb8aa3b, v134
	v_pk_mul_f32 v[102:103], v[88:89], v[100:101] op_sel_hi:[1,0]
	v_pk_mul_f32 v[104:105], v[86:87], v[100:101] op_sel_hi:[1,0]
	v_pk_mul_f32 v[106:107], v[84:85], v[100:101] op_sel_hi:[1,0]
	v_pk_mul_f32 v[100:101], v[82:83], v[100:101] op_sel_hi:[1,0]
	v_exp_f32_e32 v106, v106
	v_exp_f32_e32 v100, v100
	v_exp_f32_e32 v107, v107
	v_exp_f32_e32 v101, v101
	v_exp_f32_e32 v104, v104
	v_exp_f32_e32 v105, v105
	v_exp_f32_e32 v102, v102
	v_exp_f32_e32 v103, v103
	v_pk_add_f32 v[106:107], v[106:107], 1.0 op_sel_hi:[1,0]
	v_pk_add_f32 v[100:101], v[100:101], 1.0 op_sel_hi:[1,0]
	v_pk_add_f32 v[104:105], v[104:105], 1.0 op_sel_hi:[1,0]
	v_pk_add_f32 v[102:103], v[102:103], 1.0 op_sel_hi:[1,0]
	v_rcp_f32_e32 v100, v100
	v_rcp_f32_e32 v101, v101
	v_rcp_f32_e32 v106, v106
	v_rcp_f32_e32 v107, v107
	v_rcp_f32_e32 v104, v104
	v_rcp_f32_e32 v105, v105
	v_rcp_f32_e32 v102, v102
	v_rcp_f32_e32 v103, v103
	v_pk_mul_f32 v[84:85], v[92:93], v[84:85]
	v_pk_mul_f32 v[82:83], v[90:91], v[82:83]
	v_pk_mul_f32 v[88:89], v[96:97], v[88:89]
	v_pk_mul_f32 v[86:87], v[94:95], v[86:87]
	v_pk_mul_f32 v[84:85], v[84:85], v[108:109] op_sel_hi:[1,0]
	v_pk_mul_f32 v[82:83], v[82:83], v[108:109] op_sel_hi:[1,0]
	v_lshl_add_u64 v[98:99], v[114:115], 0, s[12:13]
	v_pk_mul_f32 v[88:89], v[88:89], v[108:109] op_sel_hi:[1,0]
	v_pk_mul_f32 v[86:87], v[86:87], v[108:109] op_sel_hi:[1,0]
	v_pk_mul_f32 v[90:91], v[84:85], v[106:107]
	v_pk_mul_f32 v[84:85], v[82:83], v[100:101]
	v_pk_mul_f32 v[88:89], v[88:89], v[102:103]
	v_pk_mul_f32 v[86:87], v[86:87], v[104:105]
	v_mul_f32_e32 v92, v135, v135
	v_cvt_pk_bf16_f32 v82, v86, v87
	v_cvt_pk_bf16_f32 v83, v88, v89
	v_cvt_pk_bf16_f32 v84, v84, v85
	v_cvt_pk_bf16_f32 v85, v90, v91
	global_store_dwordx4 v[98:99], v[82:85], off nt
	s_nop 1
	v_mul_f32_e32 v84, 0xbfb8aa3b, v135
	v_pk_mul_f32 v[86:87], v[64:65], v[84:85] op_sel_hi:[1,0]
	v_pk_mul_f32 v[88:89], v[62:63], v[84:85] op_sel_hi:[1,0]
	v_pk_mul_f32 v[90:91], v[56:57], v[84:85] op_sel_hi:[1,0]
	v_pk_mul_f32 v[84:85], v[54:55], v[84:85] op_sel_hi:[1,0]
	v_exp_f32_e32 v90, v90
	v_exp_f32_e32 v84, v84
	v_exp_f32_e32 v91, v91
	v_exp_f32_e32 v85, v85
	v_exp_f32_e32 v88, v88
	v_exp_f32_e32 v89, v89
	v_exp_f32_e32 v86, v86
	v_exp_f32_e32 v87, v87
	v_pk_add_f32 v[90:91], v[90:91], 1.0 op_sel_hi:[1,0]
	v_pk_add_f32 v[84:85], v[84:85], 1.0 op_sel_hi:[1,0]
	v_pk_add_f32 v[88:89], v[88:89], 1.0 op_sel_hi:[1,0]
	v_pk_add_f32 v[86:87], v[86:87], 1.0 op_sel_hi:[1,0]
	v_rcp_f32_e32 v84, v84
	v_rcp_f32_e32 v85, v85
	v_rcp_f32_e32 v90, v90
	v_rcp_f32_e32 v91, v91
	v_rcp_f32_e32 v88, v88
	v_rcp_f32_e32 v89, v89
	v_rcp_f32_e32 v86, v86
	v_rcp_f32_e32 v87, v87
	v_pk_mul_f32 v[56:57], v[72:73], v[56:57]
	v_pk_mul_f32 v[54:55], v[70:71], v[54:55]
	v_pk_mul_f32 v[64:65], v[80:81], v[64:65]
	v_pk_mul_f32 v[62:63], v[78:79], v[62:63]
	v_pk_mul_f32 v[56:57], v[56:57], v[92:93] op_sel_hi:[1,0]
	v_pk_mul_f32 v[54:55], v[54:55], v[92:93] op_sel_hi:[1,0]
	v_lshl_add_u64 v[82:83], v[98:99], 0, s[12:13]
	v_pk_mul_f32 v[64:65], v[64:65], v[92:93] op_sel_hi:[1,0]
	v_pk_mul_f32 v[62:63], v[62:63], v[92:93] op_sel_hi:[1,0]
	v_pk_mul_f32 v[70:71], v[56:57], v[90:91]
	v_pk_mul_f32 v[56:57], v[54:55], v[84:85]
	v_pk_mul_f32 v[64:65], v[64:65], v[86:87]
	v_pk_mul_f32 v[62:63], v[62:63], v[88:89]
	v_mul_f32_e32 v72, v132, v132
	v_cvt_pk_bf16_f32 v54, v62, v63
	v_cvt_pk_bf16_f32 v55, v64, v65
	v_cvt_pk_bf16_f32 v56, v56, v57
	v_cvt_pk_bf16_f32 v57, v70, v71
	global_store_dwordx4 v[82:83], v[54:57], off nt
	s_nop 1
	v_mul_f32_e32 v56, 0xbfb8aa3b, v132
	v_pk_mul_f32 v[62:63], v[60:61], v[56:57] op_sel_hi:[1,0]
	v_pk_mul_f32 v[64:65], v[58:59], v[56:57] op_sel_hi:[1,0]
	v_pk_mul_f32 v[70:71], v[52:53], v[56:57] op_sel_hi:[1,0]
	v_pk_mul_f32 v[56:57], v[50:51], v[56:57] op_sel_hi:[1,0]
	v_exp_f32_e32 v62, v62
	v_exp_f32_e32 v56, v56
	v_exp_f32_e32 v63, v63
	v_exp_f32_e32 v70, v70
	v_exp_f32_e32 v71, v71
	v_exp_f32_e32 v57, v57
	v_exp_f32_e32 v64, v64
	v_exp_f32_e32 v65, v65
	v_pk_add_f32 v[62:63], v[62:63], 1.0 op_sel_hi:[1,0]
	v_pk_add_f32 v[70:71], v[70:71], 1.0 op_sel_hi:[1,0]
	v_pk_add_f32 v[56:57], v[56:57], 1.0 op_sel_hi:[1,0]
	v_pk_add_f32 v[64:65], v[64:65], 1.0 op_sel_hi:[1,0]
	v_rcp_f32_e32 v56, v56
	v_rcp_f32_e32 v57, v57
	v_rcp_f32_e32 v62, v62
	v_rcp_f32_e32 v70, v70
	v_rcp_f32_e32 v63, v63
	v_rcp_f32_e32 v71, v71
	v_rcp_f32_e32 v64, v64
	v_rcp_f32_e32 v65, v65
	v_lshl_add_u64 v[54:55], v[82:83], 0, s[12:13]
	v_pk_mul_f32 v[60:61], v[76:77], v[60:61]
	v_pk_mul_f32 v[52:53], v[68:69], v[52:53]
	v_pk_mul_f32 v[50:51], v[66:67], v[50:51]
	v_pk_mul_f32 v[58:59], v[74:75], v[58:59]
	v_pk_mul_f32 v[60:61], v[60:61], v[72:73] op_sel_hi:[1,0]
	v_pk_mul_f32 v[52:53], v[52:53], v[72:73] op_sel_hi:[1,0]
	v_pk_mul_f32 v[50:51], v[50:51], v[72:73] op_sel_hi:[1,0]
	v_lshl_add_u64 v[54:55], v[54:55], 0, s[42:43]
	v_pk_mul_f32 v[58:59], v[58:59], v[72:73] op_sel_hi:[1,0]
	v_pk_mul_f32 v[60:61], v[60:61], v[62:63]
	v_pk_mul_f32 v[62:63], v[52:53], v[70:71]
	v_pk_mul_f32 v[52:53], v[50:51], v[56:57]
	v_pk_mul_f32 v[58:59], v[58:59], v[64:65]
	s_nop 0
	v_cvt_pk_bf16_f32 v50, v58, v59
	v_cvt_pk_bf16_f32 v51, v60, v61
	v_cvt_pk_bf16_f32 v52, v52, v53
	v_cvt_pk_bf16_f32 v53, v62, v63
	global_store_dwordx4 v[54:55], v[50:53], off nt
	v_mul_f32_e32 v60, v133, v133
	s_nop 0
	v_mul_f32_e32 v52, 0xbfb8aa3b, v133
	v_lshl_add_u64 v[50:51], v[54:55], 0, s[12:13]
	v_pk_mul_f32 v[54:55], v[40:41], v[52:53] op_sel_hi:[1,0]
	v_pk_mul_f32 v[56:57], v[38:39], v[52:53] op_sel_hi:[1,0]
	v_pk_mul_f32 v[58:59], v[36:37], v[52:53] op_sel_hi:[1,0]
	v_pk_mul_f32 v[52:53], v[34:35], v[52:53] op_sel_hi:[1,0]
	v_exp_f32_e32 v58, v58
	v_exp_f32_e32 v52, v52
	v_exp_f32_e32 v59, v59
	v_exp_f32_e32 v53, v53
	v_exp_f32_e32 v56, v56
	v_exp_f32_e32 v57, v57
	v_exp_f32_e32 v54, v54
	v_exp_f32_e32 v55, v55
	v_pk_add_f32 v[58:59], v[58:59], 1.0 op_sel_hi:[1,0]
	v_pk_add_f32 v[52:53], v[52:53], 1.0 op_sel_hi:[1,0]
	v_pk_add_f32 v[56:57], v[56:57], 1.0 op_sel_hi:[1,0]
	v_pk_add_f32 v[54:55], v[54:55], 1.0 op_sel_hi:[1,0]
	v_rcp_f32_e32 v52, v52
	v_rcp_f32_e32 v53, v53
	v_rcp_f32_e32 v58, v58
	v_rcp_f32_e32 v59, v59
	v_rcp_f32_e32 v56, v56
	v_rcp_f32_e32 v57, v57
	v_rcp_f32_e32 v54, v54
	v_rcp_f32_e32 v55, v55
	v_pk_mul_f32 v[36:37], v[44:45], v[36:37]
	v_pk_mul_f32 v[34:35], v[42:43], v[34:35]
	v_pk_mul_f32 v[40:41], v[48:49], v[40:41]
	v_pk_mul_f32 v[38:39], v[46:47], v[38:39]
	v_pk_mul_f32 v[36:37], v[36:37], v[60:61] op_sel_hi:[1,0]
	v_pk_mul_f32 v[34:35], v[34:35], v[60:61] op_sel_hi:[1,0]
	v_pk_mul_f32 v[40:41], v[40:41], v[60:61] op_sel_hi:[1,0]
	v_pk_mul_f32 v[38:39], v[38:39], v[60:61] op_sel_hi:[1,0]
	v_pk_mul_f32 v[42:43], v[36:37], v[58:59]
	v_pk_mul_f32 v[36:37], v[34:35], v[52:53]
	v_pk_mul_f32 v[40:41], v[40:41], v[54:55]
	v_pk_mul_f32 v[38:39], v[38:39], v[56:57]
	v_mul_f32_e32 v44, v130, v130
	v_cvt_pk_bf16_f32 v34, v38, v39
	v_cvt_pk_bf16_f32 v35, v40, v41
	v_cvt_pk_bf16_f32 v36, v36, v37
	v_cvt_pk_bf16_f32 v37, v42, v43
	global_store_dwordx4 v[50:51], v[34:37], off nt
	s_nop 1
	v_mul_f32_e32 v36, 0xbfb8aa3b, v130
	v_pk_mul_f32 v[38:39], v[24:25], v[36:37] op_sel_hi:[1,0]
	v_pk_mul_f32 v[40:41], v[22:23], v[36:37] op_sel_hi:[1,0]
	v_pk_mul_f32 v[42:43], v[20:21], v[36:37] op_sel_hi:[1,0]
	v_pk_mul_f32 v[36:37], v[18:19], v[36:37] op_sel_hi:[1,0]
	v_exp_f32_e32 v42, v42
	v_exp_f32_e32 v36, v36
	v_exp_f32_e32 v43, v43
	v_exp_f32_e32 v37, v37
	v_exp_f32_e32 v40, v40
	v_exp_f32_e32 v41, v41
	v_exp_f32_e32 v38, v38
	v_exp_f32_e32 v39, v39
	v_pk_add_f32 v[42:43], v[42:43], 1.0 op_sel_hi:[1,0]
	v_pk_add_f32 v[36:37], v[36:37], 1.0 op_sel_hi:[1,0]
	v_pk_add_f32 v[40:41], v[40:41], 1.0 op_sel_hi:[1,0]
	v_pk_add_f32 v[38:39], v[38:39], 1.0 op_sel_hi:[1,0]
	v_rcp_f32_e32 v36, v36
	v_rcp_f32_e32 v37, v37
	v_rcp_f32_e32 v42, v42
	v_rcp_f32_e32 v43, v43
	v_rcp_f32_e32 v40, v40
	v_rcp_f32_e32 v41, v41
	v_rcp_f32_e32 v38, v38
	v_rcp_f32_e32 v39, v39
	v_pk_mul_f32 v[20:21], v[28:29], v[20:21]
	v_pk_mul_f32 v[18:19], v[26:27], v[18:19]
	v_pk_mul_f32 v[24:25], v[32:33], v[24:25]
	v_pk_mul_f32 v[22:23], v[30:31], v[22:23]
	v_pk_mul_f32 v[20:21], v[20:21], v[44:45] op_sel_hi:[1,0]
	v_pk_mul_f32 v[18:19], v[18:19], v[44:45] op_sel_hi:[1,0]
	v_lshl_add_u64 v[34:35], v[50:51], 0, s[12:13]
	v_pk_mul_f32 v[24:25], v[24:25], v[44:45] op_sel_hi:[1,0]
	v_pk_mul_f32 v[22:23], v[22:23], v[44:45] op_sel_hi:[1,0]
	v_pk_mul_f32 v[26:27], v[20:21], v[42:43]
	v_pk_mul_f32 v[20:21], v[18:19], v[36:37]
	v_pk_mul_f32 v[24:25], v[24:25], v[38:39]
	v_pk_mul_f32 v[22:23], v[22:23], v[40:41]
	v_mul_f32_e32 v28, v131, v131
	v_cvt_pk_bf16_f32 v18, v22, v23
	v_cvt_pk_bf16_f32 v19, v24, v25
	v_cvt_pk_bf16_f32 v20, v20, v21
	v_cvt_pk_bf16_f32 v21, v26, v27
	global_store_dwordx4 v[34:35], v[18:21], off nt
	s_nop 1
	v_mul_f32_e32 v20, 0xbfb8aa3b, v131
	v_pk_mul_f32 v[22:23], v[8:9], v[20:21] op_sel_hi:[1,0]
	v_pk_mul_f32 v[24:25], v[6:7], v[20:21] op_sel_hi:[1,0]
	v_pk_mul_f32 v[26:27], v[4:5], v[20:21] op_sel_hi:[1,0]
	v_pk_mul_f32 v[20:21], v[2:3], v[20:21] op_sel_hi:[1,0]
	v_exp_f32_e32 v24, v24
	v_exp_f32_e32 v20, v20
	v_exp_f32_e32 v25, v25
	v_exp_f32_e32 v22, v22
	v_exp_f32_e32 v23, v23
	v_exp_f32_e32 v26, v26
	v_exp_f32_e32 v27, v27
	v_exp_f32_e32 v21, v21
	v_pk_add_f32 v[22:23], v[22:23], 1.0 op_sel_hi:[1,0]
	v_pk_add_f32 v[24:25], v[24:25], 1.0 op_sel_hi:[1,0]
	v_pk_add_f32 v[26:27], v[26:27], 1.0 op_sel_hi:[1,0]
	v_pk_add_f32 v[20:21], v[20:21], 1.0 op_sel_hi:[1,0]
	v_rcp_f32_e32 v24, v24
	v_rcp_f32_e32 v20, v20
	v_rcp_f32_e32 v25, v25
	v_rcp_f32_e32 v21, v21
	v_rcp_f32_e32 v22, v22
	v_rcp_f32_e32 v26, v26
	v_rcp_f32_e32 v23, v23
	v_rcp_f32_e32 v27, v27
	v_pk_mul_f32 v[8:9], v[16:17], v[8:9]
	v_pk_mul_f32 v[6:7], v[14:15], v[6:7]
	v_pk_mul_f32 v[4:5], v[12:13], v[4:5]
	v_pk_mul_f32 v[2:3], v[10:11], v[2:3]
	v_lshl_add_u64 v[18:19], v[34:35], 0, s[12:13]
	v_pk_mul_f32 v[8:9], v[8:9], v[28:29] op_sel_hi:[1,0]
	v_pk_mul_f32 v[6:7], v[6:7], v[28:29] op_sel_hi:[1,0]
	v_pk_mul_f32 v[4:5], v[4:5], v[28:29] op_sel_hi:[1,0]
	v_pk_mul_f32 v[2:3], v[2:3], v[28:29] op_sel_hi:[1,0]
	v_pk_mul_f32 v[8:9], v[8:9], v[22:23]
	v_pk_mul_f32 v[6:7], v[6:7], v[24:25]
	v_pk_mul_f32 v[10:11], v[4:5], v[26:27]
	v_pk_mul_f32 v[4:5], v[2:3], v[20:21]
	v_cvt_pk_bf16_f32 v2, v6, v7
	v_cvt_pk_bf16_f32 v3, v8, v9
	s_nop 0
	v_cvt_pk_bf16_f32 v4, v4, v5
	v_cvt_pk_bf16_f32 v5, v10, v11
	global_store_dwordx4 v[18:19], v[2:5], off nt
	s_nop 1
	v_lshl_add_u64 v[2:3], v[18:19], 0, s[12:13]
	s_nop 0
	v_lshl_add_u64 v[2:3], v[2:3], 0, s[42:43]
	s_cbranch_vccnz .LBB0_1138
	s_cmp_lg_u32 s76, s74
	s_cselect_b64 s[40:41], -1, 0
	v_cndmask_b32_e64 v2, 0, 1, s[40:41]
	s_andn2_b64 vcc, exec, s[30:31]
	v_readfirstlane_b32 s40, v2
	s_cbranch_vccnz .LBB0_1137
	s_barrier
	s_branch .LBB0_1137
